# speedup vs baseline: 1.0120x; 1.0008x over previous
.LBB2_12:
	s_add_i32 s16, s22, 0xffffc000
	s_and_b32 s16, s16, 0xc000
	v_add_u32_e32 v116, s16, v108
	s_add_u32 s16, s12, 0xfffce000
	s_addc_u32 s17, s13, -1
	v_readfirstlane_b32 s26, v116
	v_lshl_add_u64 v[116:117], s[16:17], 0, v[84:85]
	s_mov_b32 s27, m0
	s_mov_b32 m0, s26
	s_nop 0
	global_load_lds_dwordx4 v[116:117], off
	s_mov_b32 m0, s27
	v_lshl_add_u64 v[116:117], s[16:17], 0, v[86:87]
	s_add_i32 s16, s26, 0x400
	s_mov_b32 s17, m0
	s_mov_b32 m0, s16
	s_nop 0
	global_load_lds_dwordx4 v[116:117], off
	s_mov_b32 m0, s17
	s_and_b32 s16, s22, 0xc000
	v_add_u32_e32 v116, s16, v108
	s_nop 0
	v_readfirstlane_b32 s16, v116
	v_lshl_add_u64 v[116:117], s[12:13], 0, v[84:85]
	s_mov_b32 s17, m0
	s_mov_b32 m0, s16
	s_nop 0
	global_load_lds_dwordx4 v[116:117], off
	s_mov_b32 m0, s17
	v_lshl_add_u64 v[116:117], s[12:13], 0, v[86:87]
	s_addk_i32 s16, 0x400
	s_mov_b32 s17, m0
	s_mov_b32 m0, s16
	s_nop 0
	global_load_lds_dwordx4 v[116:117], off
	s_mov_b32 m0, s17
	v_cmp_neq_f32_e32 vcc, s25, v102
	v_add_u32_e32 v114, v114, v98
	v_add_u32_e32 v107, 2, v107
	v_cndmask_b32_e64 v124, v112, -v102, vcc
	v_fmamk_f32 v34, v34, 0x3e38aa3b, v124
	v_fmamk_f32 v50, v50, 0x3e38aa3b, v124
	v_exp_f32_e32 v126, v34
	v_fmamk_f32 v34, v51, 0x3e38aa3b, v124
	v_exp_f32_e32 v125, v50
	v_exp_f32_e32 v82, v34
	v_fmamk_f32 v34, v35, 0x3e38aa3b, v124
	v_exp_f32_e32 v34, v34
	v_add_f32_e32 v35, v126, v125
	v_fmamk_f32 v36, v36, 0x3e38aa3b, v124
	v_exp_f32_e32 v127, v36
	v_add_f32_e32 v50, v34, v82
	v_add_f32_e32 v51, v35, v83
	v_fmamk_f32 v35, v52, 0x3e38aa3b, v124
	v_add_f32_e32 v89, v50, v51
	v_fmamk_f32 v36, v53, 0x3e38aa3b, v124
	v_exp_f32_e32 v35, v35
	v_exp_f32_e32 v88, v36
	v_fmamk_f32 v36, v37, 0x3e38aa3b, v124
	v_exp_f32_e32 v36, v36
	v_add_f32_e32 v37, v127, v35
	v_fmamk_f32 v38, v38, 0x3e38aa3b, v124
	v_exp_f32_e32 v115, v38
	v_add_f32_e32 v50, v36, v88
	v_add_f32_e32 v51, v37, v89
	v_fmamk_f32 v37, v54, 0x3e38aa3b, v124
	v_add_f32_e32 v91, v50, v51
	v_fmamk_f32 v38, v55, 0x3e38aa3b, v124
	v_exp_f32_e32 v37, v37
	v_exp_f32_e32 v90, v38
	v_fmamk_f32 v38, v39, 0x3e38aa3b, v124
	v_exp_f32_e32 v50, v38
	v_add_f32_e32 v51, v115, v37
	s_add_u32 s12, s12, 0x64000
	s_addc_u32 s13, s13, 0
	v_add_f32_e32 v38, v50, v90
	v_add_f32_e32 v39, v51, v91
	s_add_i32 s22, s22, 0x8000
	v_add_f32_e32 v55, v38, v39
	v_fmamk_f32 v38, v56, 0x3e38aa3b, v124
	v_exp_f32_e32 v51, v38
	v_fmamk_f32 v38, v40, 0x3e38aa3b, v124
	v_exp_f32_e32 v91, v38
	v_fmamk_f32 v38, v57, 0x3e38aa3b, v124
	v_exp_f32_e32 v54, v38
	v_fmamk_f32 v38, v41, 0x3e38aa3b, v124
	v_exp_f32_e32 v52, v38
	v_add_f32_e32 v53, v91, v51
	v_cvt_pk_f16_f32 v57, v51, v54
	v_cvt_pk_f16_f32 v56, v37, v90
	v_add_f32_e32 v38, v52, v54
	v_add_f32_e32 v39, v53, v55
	v_cvt_pk_f16_f32 v55, v35, v88
	v_add_f32_e32 v117, v38, v39
	v_fmamk_f32 v38, v58, 0x3e38aa3b, v124
	v_exp_f32_e32 v53, v38
	v_fmamk_f32 v38, v42, 0x3e38aa3b, v124
	v_exp_f32_e32 v1, v38
	v_fmamk_f32 v38, v59, 0x3e38aa3b, v124
	v_exp_f32_e32 v116, v38
	v_fmamk_f32 v38, v43, 0x3e38aa3b, v124
	v_exp_f32_e32 v38, v38
	v_add_f32_e32 v39, v1, v53
	v_cvt_pk_f16_f32 v54, v125, v82
	v_fmamk_f32 v35, v64, 0x3e38aa3b, v124
	v_add_f32_e32 v40, v38, v116
	v_add_f32_e32 v41, v39, v117
	v_fmamk_f32 v39, v60, 0x3e38aa3b, v124
	v_add_f32_e32 v119, v40, v41
	v_fmamk_f32 v40, v44, 0x3e38aa3b, v124
	v_exp_f32_e32 v117, v40
	v_fmamk_f32 v40, v61, 0x3e38aa3b, v124
	v_exp_f32_e32 v39, v39
	v_exp_f32_e32 v118, v40
	v_fmamk_f32 v40, v45, 0x3e38aa3b, v124
	v_exp_f32_e32 v40, v40
	v_add_f32_e32 v41, v117, v39
	v_exp_f32_e32 v82, v35
	v_fmamk_f32 v35, v65, 0x3e38aa3b, v124
	v_add_f32_e32 v42, v40, v118
	v_add_f32_e32 v43, v41, v119
	v_fmamk_f32 v41, v62, 0x3e38aa3b, v124
	v_add_f32_e32 v121, v42, v43
	v_fmamk_f32 v42, v46, 0x3e38aa3b, v124
	v_exp_f32_e32 v119, v42
	v_fmamk_f32 v42, v63, 0x3e38aa3b, v124
	v_exp_f32_e32 v41, v41
	v_exp_f32_e32 v120, v42
	v_fmamk_f32 v42, v47, 0x3e38aa3b, v124
	v_exp_f32_e32 v122, v42
	ds_read_b64_tr_b16 v[42:43], v114 offset:8192
	ds_read_b64_tr_b16 v[44:45], v114 offset:8704
	v_add_f32_e32 v123, v119, v41
	ds_read_b64_tr_b16 v[58:59], v114 offset:9216
	ds_read_b64_tr_b16 v[60:61], v114 offset:9728
	v_add_f32_e32 v46, v122, v120
	v_add_f32_e32 v47, v123, v121
	s_waitcnt lgkmcnt(2)
	v_mfma_f32_32x32x16_f16 v[18:33], v[54:57], v[42:45], v[18:33]
	v_add_f32_e64 v88, v46, v46
	v_add_f32_e64 v89, v46, v47
	ds_read_b64_tr_b16 v[42:43], v114 offset:12288
	ds_read_b64_tr_b16 v[44:45], v114 offset:12800
	v_exp_f32_e32 v88, v35
	ds_read_b64_tr_b16 v[62:63], v114 offset:13312
	ds_read_b64_tr_b16 v[64:65], v114 offset:13824
	v_cvt_pk_f16_f32 v51, v127, v36
	v_cmp_le_u32_e32 vcc, s21, v107
	s_or_b64 s[14:15], vcc, s[14:15]
	s_waitcnt lgkmcnt(2)
	v_mfma_f32_32x32x16_f16 v[2:17], v[54:57], v[42:45], v[2:17]
	v_cvt_pk_f16_f32 v45, v82, v88
	v_cvt_pk_f16_f32 v44, v41, v120
	v_cvt_pk_f16_f32 v43, v39, v118
	v_cvt_pk_f16_f32 v42, v53, v116
	v_cvt_pk_f16_f32 v53, v91, v52
	v_cvt_pk_f16_f32 v52, v115, v50
	v_cvt_pk_f16_f32 v50, v126, v34
	v_mfma_f32_32x32x16_f16 v[18:33], v[42:45], v[58:61], v[18:33]
	v_fmamk_f32 v39, v48, 0x3e38aa3b, v124
	v_fmac_f32_e32 v124, 0x3e38aa3b, v49
	v_exp_f32_e32 v39, v39
	v_exp_f32_e32 v54, v124
	v_cvt_pk_f16_f32 v41, v117, v40
	v_cvt_pk_f16_f32 v40, v1, v38
	v_add_f32_e32 v55, v39, v82
	s_waitcnt lgkmcnt(0)
	v_mfma_f32_32x32x16_f16 v[2:17], v[42:45], v[62:65], v[2:17]
	ds_read_b64_tr_b16 v[42:43], v114 offset:10240
	ds_read_b64_tr_b16 v[44:45], v114 offset:10752
	ds_read_b64_tr_b16 v[34:35], v114 offset:11264
	ds_read_b64_tr_b16 v[36:37], v114 offset:11776
	s_waitcnt lgkmcnt(2)
	v_mfma_f32_32x32x16_f16 v[18:33], v[50:53], v[42:45], v[18:33]
	ds_read_b64_tr_b16 v[42:43], v114 offset:14336
	ds_read_b64_tr_b16 v[44:45], v114 offset:14848
	ds_read_b64_tr_b16 v[46:47], v114 offset:15360
	ds_read_b64_tr_b16 v[48:49], v114 offset:15872
	s_waitcnt lgkmcnt(2)
	v_mfma_f32_32x32x16_f16 v[2:17], v[50:53], v[42:45], v[2:17]
	v_cvt_pk_f16_f32 v43, v39, v54
	v_cvt_pk_f16_f32 v42, v119, v122
	s_nop 1
	v_mfma_f32_32x32x16_f16 v[18:33], v[40:43], v[34:37], v[18:33]
	v_add_f32_e64 v34, v54, v88
	v_add_f32_e64 v35, v55, v89
	v_mov_b32_e32 v88, v102
	v_add_f32_e32 v1, v34, v35
	v_add_f32_e32 v113, v113, v1
	s_waitcnt lgkmcnt(0)
	v_mfma_f32_32x32x16_f16 v[2:17], v[40:43], v[46:49], v[2:17]
	s_andn2_b64 exec, exec, s[14:15]
	s_cbranch_execz .LBB2_17
